# Z stores: write-through plus nt
# baseline (speedup 1.0000x reference)
;     __device__ __forceinline__ void operator()() { if (cnt == turn) run_all(tid_); ++cnt; }
;     __device__ __forceinline__ void operator()(const Acc& acc, const Unit& u, int wr, int wc, int fr, int fq) const {
;         const int row0 = u.pm * BM + wr * 64 + fr, col0 = u.pn * BM + wc * 32 + 8 * fq;
;         const float sc = (u.pn < 4) ? QSCALE : 1.f;
;         const bool dorope = (u.pn == 2 || u.pn == 3 || u.pn == 6 || u.pn == 7) && (u.pm * BM < NTOK);
; #pragma unroll
;         for (int ai = 0; ai < 2; ++ai)
; #pragma unroll
;             for (int m = 0; m < 4; ++m) { const int row = row0 + ai * HALF + m * 16; f16* rowp = O + (size_t)row * ZP0 + col0;
;                 const int t = row & (SEQ - 1), prow = t >> 6, pcol = t & 63;
; #pragma unroll
;                 for (int bj = 0; bj < 2; ++bj) { f32x4 v0 = acc[ai][bj][m][0] * sc, v1 = acc[ai][bj][m][1] * sc;
;                     if (dorope) { const int c = col0 + bj * HALF, half = (c >> 5) & 1, i0 = (c & 31) >> 1; const int pos = half ? pcol : prow;
;                         const f32x4* tp = (const f32x4*)(rope + (pos * 16 + i0) * 2); const f32x4 t0 = tp[0], t1 = tp[1];
;                         f32x4 r0, r1;
;                         r0[0] = v0[0] * t0[0] - v0[1] * t0[1]; r0[1] = v0[0] * t0[1] + v0[1] * t0[0];
;                         r0[2] = v0[2] * t0[2] - v0[3] * t0[3]; r0[3] = v0[2] * t0[3] + v0[3] * t0[2];
;                         r1[0] = v1[0] * t1[0] - v1[1] * t1[1]; r1[1] = v1[0] * t1[1] + v1[1] * t1[0];
;                         r1[2] = v1[2] * t1[2] - v1[3] * t1[3]; r1[3] = v1[2] * t1[3] + v1[3] * t1[2];
;                         v0 = r0; v1 = r1; }
;                     u32x4 w; w.x = pkh(v0[0], v0[1]); w.y = pkh(v0[2], v0[3]); w.z = pkh(v1[0], v1[1]); w.w = pkh(v1[2], v1[3]);
;                     *(u32x4*)(rowp + bj * HALF) = w; } }
;     }
.LBB0_391:
	v_or_b32_e32 v162, s21, v1
	v_lshl_or_b32 v122, s26, 8, v157
	v_mov_b64_e32 v[126:127], s[76:77]
	v_mov_b32_e32 v147, v146
	v_ashrrev_i32_e32 v123, 31, v122
	v_mad_i64_i32 v[126:127], s[2:3], v162, s47, v[126:127]
	v_cvt_pk_f16_f32 v167, v124, v125
	v_mov_b32_e32 v124, v146
	v_mov_b32_e32 v125, v146
	v_lshl_add_u64 v[126:127], v[122:123], 1, v[126:127]
	v_cvt_pk_f16_f32 v164, v128, v129
	v_cvt_pk_f16_f32 v165, v150, v151
	v_cvt_pk_f16_f32 v166, v148, v149
	v_pk_mul_f32 v[120:121], v[124:125], v[120:121]
	v_pk_mul_f32 v[118:119], v[146:147], v[118:119]
	v_pk_mul_f32 v[116:117], v[124:125], v[116:117]
	s_and_b64 vcc, exec, s[8:9]
	v_pk_mul_f32 v[114:115], v[146:147], v[114:115]
	global_store_dwordx4 v[126:127], v[164:167], off sc0 sc1 nt
	s_cbranch_vccnz .LBB0_393
	v_lshlrev_b32_e32 v128, 2, v163
	global_load_dwordx4 v[148:151], v128, s[12:13]
	global_load_dwordx4 v[164:167], v128, s[12:13] offset:16
	s_waitcnt vmcnt(0)
	v_pk_mul_f32 v[168:169], v[118:119], v[148:149] op_sel:[1,1] op_sel_hi:[1,0]
	v_mul_f32_e32 v170, v121, v151
	v_mul_f32_e32 v172, v121, v150
	v_pk_mul_f32 v[176:177], v[114:115], v[164:165] op_sel:[1,1] op_sel_hi:[1,0]
	v_mul_f32_e32 v178, v117, v167
	v_mul_f32_e32 v180, v117, v166
	v_pk_mul_f32 v[128:129], v[118:119], v[148:149]
	v_pk_mul_f32 v[174:175], v[114:115], v[164:165]
	v_pk_fma_f32 v[118:119], v[118:119], v[148:149], v[168:169] op_sel_hi:[0,1,1]
	v_pk_fma_f32 v[148:149], v[120:121], v[150:151], v[170:171] op_sel_hi:[1,1,0] neg_lo:[0,0,1] neg_hi:[0,0,1]
	v_pk_fma_f32 v[150:151], v[120:121], v[150:151], v[172:173] op_sel:[0,1,0] op_sel_hi:[1,0,0]
	v_pk_fma_f32 v[114:115], v[114:115], v[164:165], v[176:177] op_sel_hi:[0,1,1]
	v_pk_fma_f32 v[120:121], v[116:117], v[166:167], v[178:179] op_sel_hi:[1,1,0] neg_lo:[0,0,1] neg_hi:[0,0,1]
	v_pk_fma_f32 v[164:165], v[116:117], v[166:167], v[180:181] op_sel:[0,1,0] op_sel_hi:[1,0,0]
	v_sub_f32_e32 v114, v174, v176
	v_sub_f32_e32 v118, v128, v168
	v_mov_b32_e32 v116, v120
	v_mov_b32_e32 v117, v164
	v_mov_b32_e32 v120, v148
	v_mov_b32_e32 v121, v150
.LBB0_393:
	v_cvt_pk_f16_f32 v118, v118, v119
	v_cvt_pk_f16_f32 v119, v120, v121
	v_cvt_pk_f16_f32 v120, v114, v115
	v_mov_b32_e32 v114, s19
	v_cndmask_b32_e64 v114, v154, v114, s[4:5]
	v_cvt_pk_f16_f32 v121, v116, v117
	v_lshl_or_b32 v116, v114, 5, v152
	v_pk_mul_f32 v[114:115], v[124:125], v[112:113]
	v_pk_mul_f32 v[110:111], v[146:147], v[110:111]
	v_pk_mul_f32 v[112:113], v[124:125], v[108:109]
	s_and_b64 vcc, exec, s[8:9]
	v_pk_mul_f32 v[106:107], v[146:147], v[106:107]
	global_store_dwordx4 v[126:127], v[118:121], off offset:256 sc0 sc1 nt
	s_cbranch_vccnz .LBB0_395
	v_lshlrev_b32_e32 v108, 2, v116
	global_load_dwordx4 v[118:121], v108, s[12:13]
	global_load_dwordx4 v[124:127], v108, s[12:13] offset:16
	s_waitcnt vmcnt(0)
	v_pk_mul_f32 v[128:129], v[110:111], v[118:119] op_sel:[1,1] op_sel_hi:[1,0]
	v_mul_f32_e32 v148, v115, v121
	v_mul_f32_e32 v150, v115, v120
	v_pk_mul_f32 v[166:167], v[106:107], v[124:125] op_sel:[1,1] op_sel_hi:[1,0]
	v_mul_f32_e32 v168, v113, v127
	v_mul_f32_e32 v170, v113, v126
	v_pk_mul_f32 v[108:109], v[110:111], v[118:119]
	v_pk_mul_f32 v[164:165], v[106:107], v[124:125]
	v_pk_fma_f32 v[110:111], v[110:111], v[118:119], v[128:129] op_sel_hi:[0,1,1]
	v_pk_fma_f32 v[118:119], v[114:115], v[120:121], v[148:149] op_sel_hi:[1,1,0] neg_lo:[0,0,1] neg_hi:[0,0,1]
	v_pk_fma_f32 v[120:121], v[114:115], v[120:121], v[150:151] op_sel:[0,1,0] op_sel_hi:[1,0,0]
	v_pk_fma_f32 v[106:107], v[106:107], v[124:125], v[166:167] op_sel_hi:[0,1,1]
	v_pk_fma_f32 v[114:115], v[112:113], v[126:127], v[168:169] op_sel_hi:[1,1,0] neg_lo:[0,0,1] neg_hi:[0,0,1]
	v_pk_fma_f32 v[124:125], v[112:113], v[126:127], v[170:171] op_sel:[0,1,0] op_sel_hi:[1,0,0]
	v_sub_f32_e32 v106, v164, v166
	v_sub_f32_e32 v110, v108, v128
	v_mov_b32_e32 v112, v114
	v_mov_b32_e32 v113, v124
	v_mov_b32_e32 v114, v118
	v_mov_b32_e32 v115, v120
.LBB0_395:
	v_or_b32_e32 v117, 16, v162
	v_mov_b64_e32 v[108:109], s[76:77]
	v_mad_i64_i32 v[108:109], s[2:3], v117, s47, v[108:109]
	v_cvt_pk_f16_f32 v120, v106, v107
	v_mov_b32_e32 v106, v146
	v_mov_b32_e32 v107, v146
	v_lshl_add_u64 v[108:109], v[122:123], 1, v[108:109]
	v_cvt_pk_f16_f32 v118, v110, v111
	v_cvt_pk_f16_f32 v119, v114, v115
	v_cvt_pk_f16_f32 v121, v112, v113
	v_pk_mul_f32 v[104:105], v[106:107], v[104:105]
	v_pk_mul_f32 v[102:103], v[146:147], v[102:103]
	v_pk_mul_f32 v[100:101], v[106:107], v[100:101]
	s_and_b64 vcc, exec, s[8:9]
	v_pk_mul_f32 v[98:99], v[146:147], v[98:99]
	global_store_dwordx4 v[108:109], v[118:121], off sc0 sc1 nt
	s_cbranch_vccnz .LBB0_397
	v_lshlrev_b32_e32 v114, 2, v116
	global_load_dwordx4 v[110:113], v114, s[12:13]
	s_nop 0
	global_load_dwordx4 v[114:117], v114, s[12:13] offset:16
	s_waitcnt vmcnt(0)
	v_pk_mul_f32 v[120:121], v[102:103], v[110:111] op_sel:[1,1] op_sel_hi:[1,0]
	v_mul_f32_e32 v124, v105, v113
	v_mul_f32_e32 v126, v105, v112
	v_pk_mul_f32 v[148:149], v[98:99], v[114:115] op_sel:[1,1] op_sel_hi:[1,0]
	v_mul_f32_e32 v150, v101, v117
	v_mul_f32_e32 v164, v101, v116
	v_pk_mul_f32 v[118:119], v[102:103], v[110:111]
	v_pk_mul_f32 v[128:129], v[98:99], v[114:115]
	v_pk_fma_f32 v[102:103], v[102:103], v[110:111], v[120:121] op_sel_hi:[0,1,1]
	v_pk_fma_f32 v[110:111], v[104:105], v[112:113], v[124:125] op_sel_hi:[1,1,0] neg_lo:[0,0,1] neg_hi:[0,0,1]
	v_pk_fma_f32 v[112:113], v[104:105], v[112:113], v[126:127] op_sel:[0,1,0] op_sel_hi:[1,0,0]
	v_pk_fma_f32 v[98:99], v[98:99], v[114:115], v[148:149] op_sel_hi:[0,1,1]
	v_pk_fma_f32 v[104:105], v[100:101], v[116:117], v[150:151] op_sel_hi:[1,1,0] neg_lo:[0,0,1] neg_hi:[0,0,1]
	v_pk_fma_f32 v[114:115], v[100:101], v[116:117], v[164:165] op_sel:[0,1,0] op_sel_hi:[1,0,0]
	v_sub_f32_e32 v98, v128, v148
	v_sub_f32_e32 v102, v118, v120
	v_mov_b32_e32 v100, v104
	v_mov_b32_e32 v101, v114
	v_mov_b32_e32 v104, v110
	v_mov_b32_e32 v105, v112
;     __device__ __forceinline__ void operator()(const Acc& acc, const Unit& u, int wr, int wc, int fr, int fq) const {
;     ...
;             for (int m = 0; m < 4; ++m) { const int row = row0 + ai * HALF + m * 16; f16* rowp = O + (size_t)row * ZP0 + col0;
;                 const int t = row & (SEQ - 1), prow = t >> 6, pcol = t & 63;
; #pragma unroll
;                 for (int bj = 0; bj < 2; ++bj) { f32x4 v0 = acc[ai][bj][m][0] * sc, v1 = acc[ai][bj][m][1] * sc;
;                     if (dorope) { const int c = col0 + bj * HALF, half = (c >> 5) & 1, i0 = (c & 31) >> 1; const int pos = half ? pcol : prow;
;                         const f32x4* tp = (const f32x4*)(rope + (pos * 16 + i0) * 2); const f32x4 t0 = tp[0], t1 = tp[1];
;                         f32x4 r0, r1;
;                         r0[0] = v0[0] * t0[0] - v0[1] * t0[1]; r0[1] = v0[0] * t0[1] + v0[1] * t0[0];
;                         r0[2] = v0[2] * t0[2] - v0[3] * t0[3]; r0[3] = v0[2] * t0[3] + v0[3] * t0[2];
;                         r1[0] = v1[0] * t1[0] - v1[1] * t1[1]; r1[1] = v1[0] * t1[1] + v1[1] * t1[0];
;                         r1[2] = v1[2] * t1[2] - v1[3] * t1[3]; r1[3] = v1[2] * t1[3] + v1[3] * t1[2];
;                         v0 = r0; v1 = r1; }
;                     u32x4 w; w.x = pkh(v0[0], v0[1]); w.y = pkh(v0[2], v0[3]); w.z = pkh(v1[0], v1[1]); w.w = pkh(v1[2], v1[3]);
;                     *(u32x4*)(rowp + bj * HALF) = w; } }
.LBB0_397:
	v_cvt_pk_f16_f32 v102, v102, v103
	v_cvt_pk_f16_f32 v103, v104, v105
	v_cvt_pk_f16_f32 v104, v98, v99
	v_mov_b32_e32 v98, s19
	v_cndmask_b32_e64 v98, v155, v98, s[4:5]
	v_cvt_pk_f16_f32 v105, v100, v101
	v_lshl_or_b32 v100, v98, 5, v152
	v_pk_mul_f32 v[98:99], v[106:107], v[96:97]
	v_pk_mul_f32 v[94:95], v[146:147], v[94:95]
	v_pk_mul_f32 v[96:97], v[106:107], v[92:93]
	s_and_b64 vcc, exec, s[8:9]
	v_pk_mul_f32 v[90:91], v[146:147], v[90:91]
	global_store_dwordx4 v[108:109], v[102:105], off offset:256 sc0 sc1 nt
	s_cbranch_vccnz .LBB0_399
	v_lshlrev_b32_e32 v92, 2, v100
	global_load_dwordx4 v[102:105], v92, s[12:13]
	global_load_dwordx4 v[106:109], v92, s[12:13] offset:16
	s_waitcnt vmcnt(0)
	v_pk_mul_f32 v[110:111], v[94:95], v[102:103] op_sel:[1,1] op_sel_hi:[1,0]
	v_mul_f32_e32 v112, v99, v105
	v_mul_f32_e32 v114, v99, v104
	v_pk_mul_f32 v[118:119], v[90:91], v[106:107] op_sel:[1,1] op_sel_hi:[1,0]
	v_mul_f32_e32 v120, v97, v109
	v_mul_f32_e32 v124, v97, v108
	v_pk_mul_f32 v[92:93], v[94:95], v[102:103]
	v_pk_mul_f32 v[116:117], v[90:91], v[106:107]
	v_pk_fma_f32 v[94:95], v[94:95], v[102:103], v[110:111] op_sel_hi:[0,1,1]
	v_pk_fma_f32 v[102:103], v[98:99], v[104:105], v[112:113] op_sel_hi:[1,1,0] neg_lo:[0,0,1] neg_hi:[0,0,1]
	v_pk_fma_f32 v[104:105], v[98:99], v[104:105], v[114:115] op_sel:[0,1,0] op_sel_hi:[1,0,0]
	v_pk_fma_f32 v[90:91], v[90:91], v[106:107], v[118:119] op_sel_hi:[0,1,1]
	v_pk_fma_f32 v[98:99], v[96:97], v[108:109], v[120:121] op_sel_hi:[1,1,0] neg_lo:[0,0,1] neg_hi:[0,0,1]
	v_pk_fma_f32 v[106:107], v[96:97], v[108:109], v[124:125] op_sel:[0,1,0] op_sel_hi:[1,0,0]
	v_sub_f32_e32 v90, v116, v118
	v_sub_f32_e32 v94, v92, v110
	v_mov_b32_e32 v96, v98
	v_mov_b32_e32 v97, v106
	v_mov_b32_e32 v98, v102
	v_mov_b32_e32 v99, v104
.LBB0_399:
	v_or_b32_e32 v101, 32, v162
	v_mov_b64_e32 v[92:93], s[76:77]
	v_mad_i64_i32 v[92:93], s[2:3], v101, s47, v[92:93]
	v_cvt_pk_f16_f32 v104, v90, v91
	v_mov_b32_e32 v90, v146
	v_mov_b32_e32 v91, v146
	v_lshl_add_u64 v[92:93], v[122:123], 1, v[92:93]
	v_cvt_pk_f16_f32 v102, v94, v95
	v_cvt_pk_f16_f32 v103, v98, v99
	v_cvt_pk_f16_f32 v105, v96, v97
	v_pk_mul_f32 v[88:89], v[90:91], v[88:89]
	v_pk_mul_f32 v[86:87], v[146:147], v[86:87]
	v_pk_mul_f32 v[84:85], v[90:91], v[84:85]
	s_and_b64 vcc, exec, s[8:9]
	v_pk_mul_f32 v[82:83], v[146:147], v[82:83]
	global_store_dwordx4 v[92:93], v[102:105], off sc0 sc1 nt
	s_cbranch_vccnz .LBB0_401
	v_lshlrev_b32_e32 v98, 2, v100
	global_load_dwordx4 v[94:97], v98, s[12:13]
	s_nop 0
	global_load_dwordx4 v[98:101], v98, s[12:13] offset:16
	s_waitcnt vmcnt(0)
	v_pk_mul_f32 v[104:105], v[86:87], v[94:95] op_sel:[1,1] op_sel_hi:[1,0]
	v_mul_f32_e32 v106, v89, v97
	v_mul_f32_e32 v108, v89, v96
	v_pk_mul_f32 v[112:113], v[82:83], v[98:99] op_sel:[1,1] op_sel_hi:[1,0]
	v_mul_f32_e32 v114, v85, v101
	v_mul_f32_e32 v116, v85, v100
	v_pk_mul_f32 v[102:103], v[86:87], v[94:95]
	v_pk_mul_f32 v[110:111], v[82:83], v[98:99]
	v_pk_fma_f32 v[86:87], v[86:87], v[94:95], v[104:105] op_sel_hi:[0,1,1]
	v_pk_fma_f32 v[94:95], v[88:89], v[96:97], v[106:107] op_sel_hi:[1,1,0] neg_lo:[0,0,1] neg_hi:[0,0,1]
	v_pk_fma_f32 v[96:97], v[88:89], v[96:97], v[108:109] op_sel:[0,1,0] op_sel_hi:[1,0,0]
	v_pk_fma_f32 v[82:83], v[82:83], v[98:99], v[112:113] op_sel_hi:[0,1,1]
	v_pk_fma_f32 v[88:89], v[84:85], v[100:101], v[114:115] op_sel_hi:[1,1,0] neg_lo:[0,0,1] neg_hi:[0,0,1]
	v_pk_fma_f32 v[98:99], v[84:85], v[100:101], v[116:117] op_sel:[0,1,0] op_sel_hi:[1,0,0]
	v_sub_f32_e32 v82, v110, v112
	v_sub_f32_e32 v86, v102, v104
	v_mov_b32_e32 v84, v88
	v_mov_b32_e32 v85, v98
	v_mov_b32_e32 v88, v94
	v_mov_b32_e32 v89, v96
.LBB0_401:
	v_cvt_pk_f16_f32 v86, v86, v87
	v_cvt_pk_f16_f32 v87, v88, v89
	v_cvt_pk_f16_f32 v88, v82, v83
	v_mov_b32_e32 v82, s19
	v_cndmask_b32_e64 v82, v156, v82, s[4:5]
	v_cvt_pk_f16_f32 v89, v84, v85
	v_lshl_or_b32 v84, v82, 5, v152
	v_pk_mul_f32 v[82:83], v[90:91], v[80:81]
	v_pk_mul_f32 v[78:79], v[146:147], v[78:79]
	v_pk_mul_f32 v[80:81], v[90:91], v[76:77]
	s_and_b64 vcc, exec, s[8:9]
	v_pk_mul_f32 v[74:75], v[146:147], v[74:75]
	global_store_dwordx4 v[92:93], v[86:89], off offset:256 sc0 sc1 nt
	s_cbranch_vccnz .LBB0_403
	v_lshlrev_b32_e32 v76, 2, v84
	global_load_dwordx4 v[86:89], v76, s[12:13]
	global_load_dwordx4 v[90:93], v76, s[12:13] offset:16
	s_waitcnt vmcnt(0)
	v_pk_mul_f32 v[94:95], v[78:79], v[86:87] op_sel:[1,1] op_sel_hi:[1,0]
	v_mul_f32_e32 v96, v83, v89
	v_mul_f32_e32 v98, v83, v88
	v_pk_mul_f32 v[102:103], v[74:75], v[90:91] op_sel:[1,1] op_sel_hi:[1,0]
	v_mul_f32_e32 v104, v81, v93
	v_mul_f32_e32 v106, v81, v92
	v_pk_mul_f32 v[76:77], v[78:79], v[86:87]
	v_pk_mul_f32 v[100:101], v[74:75], v[90:91]
	v_pk_fma_f32 v[78:79], v[78:79], v[86:87], v[94:95] op_sel_hi:[0,1,1]
	v_pk_fma_f32 v[86:87], v[82:83], v[88:89], v[96:97] op_sel_hi:[1,1,0] neg_lo:[0,0,1] neg_hi:[0,0,1]
	v_pk_fma_f32 v[88:89], v[82:83], v[88:89], v[98:99] op_sel:[0,1,0] op_sel_hi:[1,0,0]
	v_pk_fma_f32 v[74:75], v[74:75], v[90:91], v[102:103] op_sel_hi:[0,1,1]
	v_pk_fma_f32 v[82:83], v[80:81], v[92:93], v[104:105] op_sel_hi:[1,1,0] neg_lo:[0,0,1] neg_hi:[0,0,1]
	v_pk_fma_f32 v[90:91], v[80:81], v[92:93], v[106:107] op_sel:[0,1,0] op_sel_hi:[1,0,0]
	v_sub_f32_e32 v74, v100, v102
	v_sub_f32_e32 v78, v76, v94
	v_mov_b32_e32 v80, v82
	v_mov_b32_e32 v81, v90
	v_mov_b32_e32 v82, v86
	v_mov_b32_e32 v83, v88
;     __device__ __forceinline__ void operator()(const Acc& acc, const Unit& u, int wr, int wc, int fr, int fq) const {
;     ...
;             for (int m = 0; m < 4; ++m) { const int row = row0 + ai * HALF + m * 16; f16* rowp = O + (size_t)row * ZP0 + col0;
;                 const int t = row & (SEQ - 1), prow = t >> 6, pcol = t & 63;
; #pragma unroll
;                 for (int bj = 0; bj < 2; ++bj) { f32x4 v0 = acc[ai][bj][m][0] * sc, v1 = acc[ai][bj][m][1] * sc;
;                     if (dorope) { const int c = col0 + bj * HALF, half = (c >> 5) & 1, i0 = (c & 31) >> 1; const int pos = half ? pcol : prow;
;                         const f32x4* tp = (const f32x4*)(rope + (pos * 16 + i0) * 2); const f32x4 t0 = tp[0], t1 = tp[1];
;                         f32x4 r0, r1;
;                         r0[0] = v0[0] * t0[0] - v0[1] * t0[1]; r0[1] = v0[0] * t0[1] + v0[1] * t0[0];
;                         r0[2] = v0[2] * t0[2] - v0[3] * t0[3]; r0[3] = v0[2] * t0[3] + v0[3] * t0[2];
;                         r1[0] = v1[0] * t1[0] - v1[1] * t1[1]; r1[1] = v1[0] * t1[1] + v1[1] * t1[0];
;                         r1[2] = v1[2] * t1[2] - v1[3] * t1[3]; r1[3] = v1[2] * t1[3] + v1[3] * t1[2];
;                         v0 = r0; v1 = r1; }
;                     u32x4 w; w.x = pkh(v0[0], v0[1]); w.y = pkh(v0[2], v0[3]); w.z = pkh(v1[0], v1[1]); w.w = pkh(v1[2], v1[3]);
;                     *(u32x4*)(rowp + bj * HALF) = w; } }
.LBB0_403:
	v_or_b32_e32 v85, 48, v162
	v_mov_b64_e32 v[76:77], s[76:77]
	v_mad_i64_i32 v[76:77], s[2:3], v85, s47, v[76:77]
	v_cvt_pk_f16_f32 v88, v74, v75
	v_mov_b32_e32 v74, v146
	v_mov_b32_e32 v75, v146
	v_lshl_add_u64 v[76:77], v[122:123], 1, v[76:77]
	v_cvt_pk_f16_f32 v86, v78, v79
	v_cvt_pk_f16_f32 v87, v82, v83
	v_cvt_pk_f16_f32 v89, v80, v81
	v_pk_mul_f32 v[72:73], v[74:75], v[72:73]
	v_pk_mul_f32 v[70:71], v[146:147], v[70:71]
	v_pk_mul_f32 v[68:69], v[74:75], v[68:69]
	s_and_b64 vcc, exec, s[8:9]
	v_pk_mul_f32 v[66:67], v[146:147], v[66:67]
	global_store_dwordx4 v[76:77], v[86:89], off sc0 sc1 nt
	s_cbranch_vccnz .LBB0_405
	v_lshlrev_b32_e32 v82, 2, v84
	global_load_dwordx4 v[78:81], v82, s[12:13]
	s_nop 0
	global_load_dwordx4 v[82:85], v82, s[12:13] offset:16
	s_waitcnt vmcnt(0)
	v_pk_mul_f32 v[88:89], v[70:71], v[78:79] op_sel:[1,1] op_sel_hi:[1,0]
	v_mul_f32_e32 v90, v73, v81
	v_mul_f32_e32 v92, v73, v80
	v_pk_mul_f32 v[96:97], v[66:67], v[82:83] op_sel:[1,1] op_sel_hi:[1,0]
	v_mul_f32_e32 v98, v69, v85
	v_mul_f32_e32 v100, v69, v84
	v_pk_mul_f32 v[86:87], v[70:71], v[78:79]
	v_pk_mul_f32 v[94:95], v[66:67], v[82:83]
	v_pk_fma_f32 v[70:71], v[70:71], v[78:79], v[88:89] op_sel_hi:[0,1,1]
	v_pk_fma_f32 v[78:79], v[72:73], v[80:81], v[90:91] op_sel_hi:[1,1,0] neg_lo:[0,0,1] neg_hi:[0,0,1]
	v_pk_fma_f32 v[80:81], v[72:73], v[80:81], v[92:93] op_sel:[0,1,0] op_sel_hi:[1,0,0]
	v_pk_fma_f32 v[66:67], v[66:67], v[82:83], v[96:97] op_sel_hi:[0,1,1]
	v_pk_fma_f32 v[72:73], v[68:69], v[84:85], v[98:99] op_sel_hi:[1,1,0] neg_lo:[0,0,1] neg_hi:[0,0,1]
	v_pk_fma_f32 v[82:83], v[68:69], v[84:85], v[100:101] op_sel:[0,1,0] op_sel_hi:[1,0,0]
	v_sub_f32_e32 v66, v94, v96
	v_sub_f32_e32 v70, v86, v88
	v_mov_b32_e32 v68, v72
	v_mov_b32_e32 v69, v82
	v_mov_b32_e32 v72, v78
	v_mov_b32_e32 v73, v80
.LBB0_405:
	v_cvt_pk_f16_f32 v70, v70, v71
	v_cvt_pk_f16_f32 v71, v72, v73
	v_cvt_pk_f16_f32 v72, v66, v67
	v_cvt_pk_f16_f32 v73, v68, v69
	global_store_dwordx4 v[76:77], v[70:73], off offset:256 sc0 sc1 nt
	v_pk_mul_f32 v[62:63], v[146:147], v[62:63]
	s_and_b64 vcc, exec, s[8:9]
	v_add_u32_e32 v70, 0x80, v162
	v_bfe_u32 v68, v70, 6, 5
	v_cndmask_b32_e64 v66, v1, v68, s[4:5]
	v_lshl_or_b32 v69, v66, 5, v152
	v_pk_mul_f32 v[66:67], v[74:75], v[64:65]
	v_pk_mul_f32 v[64:65], v[74:75], v[60:61]
	v_pk_mul_f32 v[60:61], v[146:147], v[58:59]
	s_cbranch_vccnz .LBB0_407
	v_lshlrev_b32_e32 v58, 2, v69
	global_load_dwordx4 v[72:75], v58, s[12:13]
	global_load_dwordx4 v[76:79], v58, s[12:13] offset:16
	s_waitcnt vmcnt(0)
	v_pk_mul_f32 v[80:81], v[62:63], v[72:73] op_sel:[1,1] op_sel_hi:[1,0]
	v_mul_f32_e32 v82, v67, v75
	v_mul_f32_e32 v84, v67, v74
	v_pk_mul_f32 v[88:89], v[60:61], v[76:77] op_sel:[1,1] op_sel_hi:[1,0]
	v_mul_f32_e32 v90, v65, v79
	v_mul_f32_e32 v92, v65, v78
	v_pk_mul_f32 v[58:59], v[62:63], v[72:73]
	v_pk_mul_f32 v[86:87], v[60:61], v[76:77]
	v_pk_fma_f32 v[62:63], v[62:63], v[72:73], v[80:81] op_sel_hi:[0,1,1]
	v_pk_fma_f32 v[72:73], v[66:67], v[74:75], v[82:83] op_sel_hi:[1,1,0] neg_lo:[0,0,1] neg_hi:[0,0,1]
	v_pk_fma_f32 v[74:75], v[66:67], v[74:75], v[84:85] op_sel:[0,1,0] op_sel_hi:[1,0,0]
	v_pk_fma_f32 v[60:61], v[60:61], v[76:77], v[88:89] op_sel_hi:[0,1,1]
	v_pk_fma_f32 v[66:67], v[64:65], v[78:79], v[90:91] op_sel_hi:[1,1,0] neg_lo:[0,0,1] neg_hi:[0,0,1]
	v_pk_fma_f32 v[76:77], v[64:65], v[78:79], v[92:93] op_sel:[0,1,0] op_sel_hi:[1,0,0]
	v_sub_f32_e32 v60, v86, v88
	v_sub_f32_e32 v62, v58, v80
	v_mov_b32_e32 v64, v66
	v_mov_b32_e32 v65, v76
	v_mov_b32_e32 v66, v72
	v_mov_b32_e32 v67, v74
.LBB0_407:
	v_mov_b64_e32 v[58:59], s[76:77]
	v_mad_i64_i32 v[58:59], s[2:3], v70, s47, v[58:59]
	v_cvt_pk_f16_f32 v72, v60, v61
	v_mov_b32_e32 v60, v146
	v_mov_b32_e32 v61, v146
	v_lshl_add_u64 v[58:59], v[122:123], 1, v[58:59]
	v_cvt_pk_f16_f32 v70, v62, v63
	v_cvt_pk_f16_f32 v71, v66, v67
	v_cvt_pk_f16_f32 v73, v64, v65
	v_pk_mul_f32 v[56:57], v[60:61], v[56:57]
	v_pk_mul_f32 v[54:55], v[146:147], v[54:55]
	v_pk_mul_f32 v[52:53], v[60:61], v[52:53]
	s_and_b64 vcc, exec, s[8:9]
	v_pk_mul_f32 v[50:51], v[146:147], v[50:51]
	global_store_dwordx4 v[58:59], v[70:73], off sc0 sc1 nt
	s_cbranch_vccnz .LBB0_409
	v_lshlrev_b32_e32 v66, 2, v69
	global_load_dwordx4 v[62:65], v66, s[12:13]
	global_load_dwordx4 v[70:73], v66, s[12:13] offset:16
	s_waitcnt vmcnt(0)
	v_pk_mul_f32 v[74:75], v[54:55], v[62:63] op_sel:[1,1] op_sel_hi:[1,0]
	v_mul_f32_e32 v76, v57, v65
	v_mul_f32_e32 v78, v57, v64
	v_pk_mul_f32 v[82:83], v[50:51], v[70:71] op_sel:[1,1] op_sel_hi:[1,0]
	v_mul_f32_e32 v84, v53, v73
	v_mul_f32_e32 v86, v53, v72
	v_pk_mul_f32 v[66:67], v[54:55], v[62:63]
	v_pk_mul_f32 v[80:81], v[50:51], v[70:71]
	v_pk_fma_f32 v[54:55], v[54:55], v[62:63], v[74:75] op_sel_hi:[0,1,1]
	v_pk_fma_f32 v[62:63], v[56:57], v[64:65], v[76:77] op_sel_hi:[1,1,0] neg_lo:[0,0,1] neg_hi:[0,0,1]
	v_pk_fma_f32 v[64:65], v[56:57], v[64:65], v[78:79] op_sel:[0,1,0] op_sel_hi:[1,0,0]
	v_pk_fma_f32 v[50:51], v[50:51], v[70:71], v[82:83] op_sel_hi:[0,1,1]
	v_pk_fma_f32 v[56:57], v[52:53], v[72:73], v[84:85] op_sel_hi:[1,1,0] neg_lo:[0,0,1] neg_hi:[0,0,1]
	v_pk_fma_f32 v[70:71], v[52:53], v[72:73], v[86:87] op_sel:[0,1,0] op_sel_hi:[1,0,0]
	v_sub_f32_e32 v50, v80, v82
	v_sub_f32_e32 v54, v66, v74
	v_mov_b32_e32 v52, v56
	v_mov_b32_e32 v53, v70
	v_mov_b32_e32 v56, v62
	v_mov_b32_e32 v57, v64
;     __device__ __forceinline__ void operator()(const Acc& acc, const Unit& u, int wr, int wc, int fr, int fq) const {
;     ...
;             for (int m = 0; m < 4; ++m) { const int row = row0 + ai * HALF + m * 16; f16* rowp = O + (size_t)row * ZP0 + col0;
;                 const int t = row & (SEQ - 1), prow = t >> 6, pcol = t & 63;
; #pragma unroll
;                 for (int bj = 0; bj < 2; ++bj) { f32x4 v0 = acc[ai][bj][m][0] * sc, v1 = acc[ai][bj][m][1] * sc;
;                     if (dorope) { const int c = col0 + bj * HALF, half = (c >> 5) & 1, i0 = (c & 31) >> 1; const int pos = half ? pcol : prow;
;                         const f32x4* tp = (const f32x4*)(rope + (pos * 16 + i0) * 2); const f32x4 t0 = tp[0], t1 = tp[1];
;                         f32x4 r0, r1;
;                         r0[0] = v0[0] * t0[0] - v0[1] * t0[1]; r0[1] = v0[0] * t0[1] + v0[1] * t0[0];
;                         r0[2] = v0[2] * t0[2] - v0[3] * t0[3]; r0[3] = v0[2] * t0[3] + v0[3] * t0[2];
;                         r1[0] = v1[0] * t1[0] - v1[1] * t1[1]; r1[1] = v1[0] * t1[1] + v1[1] * t1[0];
;                         r1[2] = v1[2] * t1[2] - v1[3] * t1[3]; r1[3] = v1[2] * t1[3] + v1[3] * t1[2];
;                         v0 = r0; v1 = r1; }
;                     u32x4 w; w.x = pkh(v0[0], v0[1]); w.y = pkh(v0[2], v0[3]); w.z = pkh(v1[0], v1[1]); w.w = pkh(v1[2], v1[3]);
;                     *(u32x4*)(rowp + bj * HALF) = w; } }
.LBB0_409:
	v_cvt_pk_f16_f32 v54, v54, v55
	v_cvt_pk_f16_f32 v55, v56, v57
	v_cvt_pk_f16_f32 v56, v50, v51
	v_cndmask_b32_e64 v50, v154, v68, s[4:5]
	v_cvt_pk_f16_f32 v57, v52, v53
	v_lshl_or_b32 v52, v50, 5, v152
	v_pk_mul_f32 v[50:51], v[60:61], v[48:49]
	v_pk_mul_f32 v[46:47], v[146:147], v[46:47]
	v_pk_mul_f32 v[48:49], v[60:61], v[44:45]
	s_and_b64 vcc, exec, s[8:9]
	v_pk_mul_f32 v[44:45], v[146:147], v[42:43]
	global_store_dwordx4 v[58:59], v[54:57], off offset:256 sc0 sc1 nt
	s_cbranch_vccnz .LBB0_411
	v_lshlrev_b32_e32 v42, 2, v52
	global_load_dwordx4 v[54:57], v42, s[12:13]
	global_load_dwordx4 v[58:61], v42, s[12:13] offset:16
	s_waitcnt vmcnt(0)
	v_pk_mul_f32 v[62:63], v[46:47], v[54:55] op_sel:[1,1] op_sel_hi:[1,0]
	v_mul_f32_e32 v64, v51, v57
	v_mul_f32_e32 v66, v51, v56
	v_pk_mul_f32 v[72:73], v[44:45], v[58:59] op_sel:[1,1] op_sel_hi:[1,0]
	v_mul_f32_e32 v74, v49, v61
	v_mul_f32_e32 v76, v49, v60
	v_pk_mul_f32 v[42:43], v[46:47], v[54:55]
	v_pk_mul_f32 v[70:71], v[44:45], v[58:59]
	v_pk_fma_f32 v[46:47], v[46:47], v[54:55], v[62:63] op_sel_hi:[0,1,1]
	v_pk_fma_f32 v[54:55], v[50:51], v[56:57], v[64:65] op_sel_hi:[1,1,0] neg_lo:[0,0,1] neg_hi:[0,0,1]
	v_pk_fma_f32 v[56:57], v[50:51], v[56:57], v[66:67] op_sel:[0,1,0] op_sel_hi:[1,0,0]
	v_pk_fma_f32 v[44:45], v[44:45], v[58:59], v[72:73] op_sel_hi:[0,1,1]
	v_pk_fma_f32 v[50:51], v[48:49], v[60:61], v[74:75] op_sel_hi:[1,1,0] neg_lo:[0,0,1] neg_hi:[0,0,1]
	v_pk_fma_f32 v[58:59], v[48:49], v[60:61], v[76:77] op_sel:[0,1,0] op_sel_hi:[1,0,0]
	v_sub_f32_e32 v44, v70, v72
	v_sub_f32_e32 v46, v42, v62
	v_mov_b32_e32 v48, v50
	v_mov_b32_e32 v49, v58
	v_mov_b32_e32 v50, v54
	v_mov_b32_e32 v51, v56
.LBB0_411:
	v_add_u32_e32 v53, 0x90, v162
	v_mov_b64_e32 v[42:43], s[76:77]
	v_mad_i64_i32 v[42:43], s[2:3], v53, s47, v[42:43]
	v_cvt_pk_f16_f32 v56, v44, v45
	v_mov_b32_e32 v44, v146
	v_mov_b32_e32 v45, v146
	v_lshl_add_u64 v[42:43], v[122:123], 1, v[42:43]
	v_cvt_pk_f16_f32 v54, v46, v47
	v_cvt_pk_f16_f32 v55, v50, v51
	v_cvt_pk_f16_f32 v57, v48, v49
	v_pk_mul_f32 v[40:41], v[44:45], v[40:41]
	v_pk_mul_f32 v[38:39], v[146:147], v[38:39]
	v_pk_mul_f32 v[36:37], v[44:45], v[36:37]
	s_and_b64 vcc, exec, s[8:9]
	v_pk_mul_f32 v[34:35], v[146:147], v[34:35]
	global_store_dwordx4 v[42:43], v[54:57], off sc0 sc1 nt
	s_cbranch_vccnz .LBB0_413
	v_lshlrev_b32_e32 v50, 2, v52
	global_load_dwordx4 v[46:49], v50, s[12:13]
	s_nop 0
	global_load_dwordx4 v[50:53], v50, s[12:13] offset:16
	s_waitcnt vmcnt(0)
	v_pk_mul_f32 v[56:57], v[38:39], v[46:47] op_sel:[1,1] op_sel_hi:[1,0]
	v_mul_f32_e32 v58, v41, v49
	v_mul_f32_e32 v60, v41, v48
	v_pk_mul_f32 v[64:65], v[34:35], v[50:51] op_sel:[1,1] op_sel_hi:[1,0]
	v_mul_f32_e32 v66, v37, v53
	v_mul_f32_e32 v70, v37, v52
	v_pk_mul_f32 v[54:55], v[38:39], v[46:47]
	v_pk_mul_f32 v[62:63], v[34:35], v[50:51]
	v_pk_fma_f32 v[38:39], v[38:39], v[46:47], v[56:57] op_sel_hi:[0,1,1]
	v_pk_fma_f32 v[46:47], v[40:41], v[48:49], v[58:59] op_sel_hi:[1,1,0] neg_lo:[0,0,1] neg_hi:[0,0,1]
	v_pk_fma_f32 v[48:49], v[40:41], v[48:49], v[60:61] op_sel:[0,1,0] op_sel_hi:[1,0,0]
	v_pk_fma_f32 v[34:35], v[34:35], v[50:51], v[64:65] op_sel_hi:[0,1,1]
	v_pk_fma_f32 v[40:41], v[36:37], v[52:53], v[66:67] op_sel_hi:[1,1,0] neg_lo:[0,0,1] neg_hi:[0,0,1]
	v_pk_fma_f32 v[50:51], v[36:37], v[52:53], v[70:71] op_sel:[0,1,0] op_sel_hi:[1,0,0]
	v_sub_f32_e32 v34, v62, v64
	v_sub_f32_e32 v38, v54, v56
	v_mov_b32_e32 v36, v40
	v_mov_b32_e32 v37, v50
	v_mov_b32_e32 v40, v46
	v_mov_b32_e32 v41, v48
.LBB0_413:
	v_cvt_pk_f16_f32 v38, v38, v39
	v_cvt_pk_f16_f32 v39, v40, v41
	v_cvt_pk_f16_f32 v40, v34, v35
	v_cndmask_b32_e64 v34, v155, v68, s[4:5]
	v_cvt_pk_f16_f32 v41, v36, v37
	v_lshl_or_b32 v36, v34, 5, v152
	v_pk_mul_f32 v[34:35], v[44:45], v[32:33]
	v_pk_mul_f32 v[30:31], v[146:147], v[30:31]
	v_pk_mul_f32 v[32:33], v[44:45], v[28:29]
	s_and_b64 vcc, exec, s[8:9]
	v_pk_mul_f32 v[28:29], v[146:147], v[26:27]
	global_store_dwordx4 v[42:43], v[38:41], off offset:256 sc0 sc1 nt
	s_cbranch_vccnz .LBB0_415
	v_lshlrev_b32_e32 v26, 2, v36
	global_load_dwordx4 v[38:41], v26, s[12:13]
	global_load_dwordx4 v[42:45], v26, s[12:13] offset:16
	s_waitcnt vmcnt(0)
	v_pk_mul_f32 v[46:47], v[30:31], v[38:39] op_sel:[1,1] op_sel_hi:[1,0]
	v_mul_f32_e32 v48, v35, v41
	v_mul_f32_e32 v50, v35, v40
	v_pk_mul_f32 v[54:55], v[28:29], v[42:43] op_sel:[1,1] op_sel_hi:[1,0]
	v_mul_f32_e32 v56, v33, v45
	v_mul_f32_e32 v58, v33, v44
	v_pk_mul_f32 v[26:27], v[30:31], v[38:39]
	v_pk_mul_f32 v[52:53], v[28:29], v[42:43]
	v_pk_fma_f32 v[30:31], v[30:31], v[38:39], v[46:47] op_sel_hi:[0,1,1]
	v_pk_fma_f32 v[38:39], v[34:35], v[40:41], v[48:49] op_sel_hi:[1,1,0] neg_lo:[0,0,1] neg_hi:[0,0,1]
	v_pk_fma_f32 v[40:41], v[34:35], v[40:41], v[50:51] op_sel:[0,1,0] op_sel_hi:[1,0,0]
	v_pk_fma_f32 v[28:29], v[28:29], v[42:43], v[54:55] op_sel_hi:[0,1,1]
	v_pk_fma_f32 v[34:35], v[32:33], v[44:45], v[56:57] op_sel_hi:[1,1,0] neg_lo:[0,0,1] neg_hi:[0,0,1]
	v_pk_fma_f32 v[42:43], v[32:33], v[44:45], v[58:59] op_sel:[0,1,0] op_sel_hi:[1,0,0]
	v_sub_f32_e32 v28, v52, v54
	v_sub_f32_e32 v30, v26, v46
	v_mov_b32_e32 v32, v34
	v_mov_b32_e32 v33, v42
	v_mov_b32_e32 v34, v38
	v_mov_b32_e32 v35, v40
; #define GM_BAR __builtin_amdgcn_s_barrier()
;     __device__ __forceinline__ void operator()(const Acc& acc, const Unit& u, int wr, int wc, int fr, int fq) const {
;     ...
;             for (int m = 0; m < 4; ++m) { const int row = row0 + ai * HALF + m * 16; f16* rowp = O + (size_t)row * ZP0 + col0;
;                 const int t = row & (SEQ - 1), prow = t >> 6, pcol = t & 63;
; #pragma unroll
;                 for (int bj = 0; bj < 2; ++bj) { f32x4 v0 = acc[ai][bj][m][0] * sc, v1 = acc[ai][bj][m][1] * sc;
;                     if (dorope) { const int c = col0 + bj * HALF, half = (c >> 5) & 1, i0 = (c & 31) >> 1; const int pos = half ? pcol : prow;
;                         const f32x4* tp = (const f32x4*)(rope + (pos * 16 + i0) * 2); const f32x4 t0 = tp[0], t1 = tp[1];
;                         f32x4 r0, r1;
;                         r0[0] = v0[0] * t0[0] - v0[1] * t0[1]; r0[1] = v0[0] * t0[1] + v0[1] * t0[0];
;                         r0[2] = v0[2] * t0[2] - v0[3] * t0[3]; r0[3] = v0[2] * t0[3] + v0[3] * t0[2];
;                         r1[0] = v1[0] * t1[0] - v1[1] * t1[1]; r1[1] = v1[0] * t1[1] + v1[1] * t1[0];
;                         r1[2] = v1[2] * t1[2] - v1[3] * t1[3]; r1[3] = v1[2] * t1[3] + v1[3] * t1[2];
;                         v0 = r0; v1 = r1; }
;                     u32x4 w; w.x = pkh(v0[0], v0[1]); w.y = pkh(v0[2], v0[3]); w.z = pkh(v1[0], v1[1]); w.w = pkh(v1[2], v1[3]);
;                     *(u32x4*)(rowp + bj * HALF) = w; } }
; template <bool BF, bool GATHER = false, class Epi, class Hook>
; __device__ __forceinline__ void gemm_phase(LAS unsigned char* lds, const Gemm g, const Order& S, const Epi& E, Hook& HK) {
;     ...
;         if (!has_next) break;
; #pragma unroll
;         for (int a = 0; a < 2; ++a)
; #pragma unroll
;             for (int b = 0; b < 2; ++b)
; #pragma unroll
;                 for (int m = 0; m < 4; ++m)
; #pragma unroll
;                     for (int n = 0; n < 2; ++n) acc[a][b][m][n] = (f32x4){0.f, 0.f, 0.f, 0.f};
;         cur = nxt; cA = nA; cB = nB; ++ui;
;         if constexpr (GATHER) { gA0[0] = nA0[0]; gA0[1] = nA0[1]; gA1[0] = nA1[0]; gA1[1] = nA1[1]; }
;         if (wr == 1) GM_BAR;
.LBB0_415:
	v_add_u32_e32 v37, 0xa0, v162
	v_mov_b64_e32 v[26:27], s[76:77]
	v_mad_i64_i32 v[26:27], s[2:3], v37, s47, v[26:27]
	v_cvt_pk_f16_f32 v40, v28, v29
	v_mov_b32_e32 v28, v146
	v_mov_b32_e32 v29, v146
	v_lshl_add_u64 v[26:27], v[122:123], 1, v[26:27]
	v_cvt_pk_f16_f32 v38, v30, v31
	v_cvt_pk_f16_f32 v39, v34, v35
	v_cvt_pk_f16_f32 v41, v32, v33
	v_pk_mul_f32 v[24:25], v[28:29], v[24:25]
	v_pk_mul_f32 v[22:23], v[146:147], v[22:23]
	v_pk_mul_f32 v[20:21], v[28:29], v[20:21]
	s_and_b64 vcc, exec, s[8:9]
	v_pk_mul_f32 v[18:19], v[146:147], v[18:19]
	global_store_dwordx4 v[26:27], v[38:41], off sc0 sc1 nt
	s_cbranch_vccnz .LBB0_417
	v_lshlrev_b32_e32 v34, 2, v36
	global_load_dwordx4 v[30:33], v34, s[12:13]
	s_nop 0
	global_load_dwordx4 v[34:37], v34, s[12:13] offset:16
	s_waitcnt vmcnt(0)
	v_pk_mul_f32 v[40:41], v[22:23], v[30:31] op_sel:[1,1] op_sel_hi:[1,0]
	v_mul_f32_e32 v42, v25, v33
	v_mul_f32_e32 v44, v25, v32
	v_pk_mul_f32 v[48:49], v[18:19], v[34:35] op_sel:[1,1] op_sel_hi:[1,0]
	v_mul_f32_e32 v50, v21, v37
	v_mul_f32_e32 v52, v21, v36
	v_pk_mul_f32 v[38:39], v[22:23], v[30:31]
	v_pk_mul_f32 v[46:47], v[18:19], v[34:35]
	v_pk_fma_f32 v[22:23], v[22:23], v[30:31], v[40:41] op_sel_hi:[0,1,1]
	v_pk_fma_f32 v[30:31], v[24:25], v[32:33], v[42:43] op_sel_hi:[1,1,0] neg_lo:[0,0,1] neg_hi:[0,0,1]
	v_pk_fma_f32 v[32:33], v[24:25], v[32:33], v[44:45] op_sel:[0,1,0] op_sel_hi:[1,0,0]
	v_pk_fma_f32 v[18:19], v[18:19], v[34:35], v[48:49] op_sel_hi:[0,1,1]
	v_pk_fma_f32 v[24:25], v[20:21], v[36:37], v[50:51] op_sel_hi:[1,1,0] neg_lo:[0,0,1] neg_hi:[0,0,1]
	v_pk_fma_f32 v[34:35], v[20:21], v[36:37], v[52:53] op_sel:[0,1,0] op_sel_hi:[1,0,0]
	v_sub_f32_e32 v18, v46, v48
	v_sub_f32_e32 v22, v38, v40
	v_mov_b32_e32 v20, v24
	v_mov_b32_e32 v21, v34
	v_mov_b32_e32 v24, v30
	v_mov_b32_e32 v25, v32
.LBB0_417:
	v_cvt_pk_f16_f32 v22, v22, v23
	v_cvt_pk_f16_f32 v23, v24, v25
	v_cvt_pk_f16_f32 v24, v18, v19
	v_cndmask_b32_e64 v18, v156, v68, s[4:5]
	v_cvt_pk_f16_f32 v25, v20, v21
	v_lshl_or_b32 v20, v18, 5, v152
	v_pk_mul_f32 v[18:19], v[28:29], v[16:17]
	v_pk_mul_f32 v[14:15], v[146:147], v[14:15]
	v_pk_mul_f32 v[16:17], v[28:29], v[12:13]
	s_and_b64 vcc, exec, s[8:9]
	v_pk_mul_f32 v[12:13], v[146:147], v[10:11]
	global_store_dwordx4 v[26:27], v[22:25], off offset:256 sc0 sc1 nt
	s_cbranch_vccnz .LBB0_419
	v_lshlrev_b32_e32 v10, 2, v20
	global_load_dwordx4 v[22:25], v10, s[12:13]
	global_load_dwordx4 v[26:29], v10, s[12:13] offset:16
	s_waitcnt vmcnt(0)
	v_pk_mul_f32 v[30:31], v[14:15], v[22:23] op_sel:[1,1] op_sel_hi:[1,0]
	v_mul_f32_e32 v32, v19, v25
	v_mul_f32_e32 v34, v19, v24
	v_pk_mul_f32 v[38:39], v[12:13], v[26:27] op_sel:[1,1] op_sel_hi:[1,0]
	v_mul_f32_e32 v40, v17, v29
	v_mul_f32_e32 v42, v17, v28
	v_pk_mul_f32 v[10:11], v[14:15], v[22:23]
	v_pk_mul_f32 v[36:37], v[12:13], v[26:27]
	v_pk_fma_f32 v[14:15], v[14:15], v[22:23], v[30:31] op_sel_hi:[0,1,1]
	v_pk_fma_f32 v[22:23], v[18:19], v[24:25], v[32:33] op_sel_hi:[1,1,0] neg_lo:[0,0,1] neg_hi:[0,0,1]
	v_pk_fma_f32 v[24:25], v[18:19], v[24:25], v[34:35] op_sel:[0,1,0] op_sel_hi:[1,0,0]
	v_pk_fma_f32 v[12:13], v[12:13], v[26:27], v[38:39] op_sel_hi:[0,1,1]
	v_pk_fma_f32 v[18:19], v[16:17], v[28:29], v[40:41] op_sel_hi:[1,1,0] neg_lo:[0,0,1] neg_hi:[0,0,1]
	v_pk_fma_f32 v[26:27], v[16:17], v[28:29], v[42:43] op_sel:[0,1,0] op_sel_hi:[1,0,0]
	v_sub_f32_e32 v12, v36, v38
	v_sub_f32_e32 v14, v10, v30
	v_mov_b32_e32 v16, v18
	v_mov_b32_e32 v17, v26
	v_mov_b32_e32 v18, v22
	v_mov_b32_e32 v19, v24
.LBB0_419:
	v_add_u32_e32 v21, 0xb0, v162
	v_mov_b64_e32 v[10:11], s[76:77]
	v_mad_i64_i32 v[10:11], s[2:3], v21, s47, v[10:11]
	v_cvt_pk_f16_f32 v24, v12, v13
	v_mov_b32_e32 v12, v146
	v_mov_b32_e32 v13, v146
	v_lshl_add_u64 v[10:11], v[122:123], 1, v[10:11]
	v_cvt_pk_f16_f32 v22, v14, v15
	v_cvt_pk_f16_f32 v23, v18, v19
	v_cvt_pk_f16_f32 v25, v16, v17
	v_pk_mul_f32 v[8:9], v[12:13], v[8:9]
	v_pk_mul_f32 v[6:7], v[146:147], v[6:7]
	v_pk_mul_f32 v[4:5], v[12:13], v[4:5]
	s_and_b64 vcc, exec, s[8:9]
	v_pk_mul_f32 v[2:3], v[146:147], v[2:3]
	global_store_dwordx4 v[10:11], v[22:25], off sc0 sc1 nt
	s_cbranch_vccnz .LBB0_421
	v_lshlrev_b32_e32 v16, 2, v20
	global_load_dwordx4 v[12:15], v16, s[12:13]
	s_nop 0
	global_load_dwordx4 v[16:19], v16, s[12:13] offset:16
	s_waitcnt vmcnt(0)
	v_pk_mul_f32 v[22:23], v[6:7], v[12:13] op_sel:[1,1] op_sel_hi:[1,0]
	v_mul_f32_e32 v24, v9, v15
	v_mul_f32_e32 v26, v9, v14
	v_pk_mul_f32 v[30:31], v[2:3], v[16:17] op_sel:[1,1] op_sel_hi:[1,0]
	v_mul_f32_e32 v32, v5, v19
	v_mul_f32_e32 v34, v5, v18
	v_pk_mul_f32 v[20:21], v[6:7], v[12:13]
	v_pk_mul_f32 v[28:29], v[2:3], v[16:17]
	v_pk_fma_f32 v[6:7], v[6:7], v[12:13], v[22:23] op_sel_hi:[0,1,1]
	v_pk_fma_f32 v[12:13], v[8:9], v[14:15], v[24:25] op_sel_hi:[1,1,0] neg_lo:[0,0,1] neg_hi:[0,0,1]
	v_pk_fma_f32 v[14:15], v[8:9], v[14:15], v[26:27] op_sel:[0,1,0] op_sel_hi:[1,0,0]
	v_pk_fma_f32 v[2:3], v[2:3], v[16:17], v[30:31] op_sel_hi:[0,1,1]
	v_pk_fma_f32 v[8:9], v[4:5], v[18:19], v[32:33] op_sel_hi:[1,1,0] neg_lo:[0,0,1] neg_hi:[0,0,1]
	v_pk_fma_f32 v[16:17], v[4:5], v[18:19], v[34:35] op_sel:[0,1,0] op_sel_hi:[1,0,0]
	v_sub_f32_e32 v2, v28, v30
	v_sub_f32_e32 v6, v20, v22
	v_mov_b32_e32 v4, v8
	v_mov_b32_e32 v5, v16
	v_mov_b32_e32 v8, v12
	v_mov_b32_e32 v9, v14
.LBB0_421:
	v_cvt_pk_f16_f32 v6, v6, v7
	v_cvt_pk_f16_f32 v7, v8, v9
	v_cvt_pk_f16_f32 v8, v2, v3
	v_cvt_pk_f16_f32 v9, v4, v5
	s_andn2_b64 vcc, exec, s[6:7]
	s_mov_b64 s[2:3], -1
	global_store_dwordx4 v[10:11], v[6:9], off offset:256 sc0 sc1 nt
	s_cbranch_vccnz .LBB0_376
	s_andn2_b64 vcc, exec, s[10:11]
	s_cbranch_vccnz .LBB0_375
	s_barrier
	s_branch .LBB0_375
